# prologue: the three small weight re-layout loops unrolled with all loads in flight (on top of v36)
# baseline (speedup 1.0000x reference)
.LBB0_43:
	s_lshl_b32 s21, s13, 6
	v_add_u32_e32 v2, s21, v71
	s_ashr_i32 s13, s12, 31
	v_ashrrev_i32_e32 v3, 31, v2
	s_lshl_b64 s[0:1], s[12:13], 9
	s_ashr_i32 s15, s14, 31
	v_lshl_add_u64 v[20:21], s[0:1], 0, v[2:3]
	s_mov_b64 s[0:1], 0x100000
	s_lshl_b64 s[16:17], s[14:15], 9
	v_cmp_gt_u64_e32 vcc, s[0:1], v[20:21]
	s_and_saveexec_b64 s[0:1], vcc
	s_cbranch_execz .LBB0_46
	s_lshl_b64 s[2:3], s[12:13], 10
	s_add_u32 s2, s10, s2
	s_addc_u32 s3, s11, s3
	v_readlane_b32 s36, v253, 26
	v_lshl_add_u64 v[4:5], v[2:3], 1, s[2:3]
	s_mov_b64 s[2:3], 0xa500000
	s_lshl_b64 s[18:19], s[12:13], 15
	v_lshlrev_b64 v[6:7], 6, v[2:3]
	v_readlane_b32 s38, v253, 28
	v_readlane_b32 s39, v253, 29
	v_readlane_b32 s42, v253, 32
	v_readlane_b32 s43, v253, 33
	v_lshl_add_u64 v[4:5], v[4:5], 0, s[2:3]
	s_lshl_b64 s[2:3], s[14:15], 10
	v_lshl_add_u64 v[6:7], s[18:19], 0, v[6:7]
	s_lshl_b64 s[18:19], s[14:15], 15
	s_mov_b64 s[28:29], 0
	v_mov_b32_e32 v9, 0
	v_mov_b32_e32 v1, s43
	v_mov_b32_e32 v12, s39
	v_mov_b32_e32 v13, s42
	v_mov_b32_e32 v14, s38
	s_movk_i32 s22, 0x7fff
	s_mov_b64 s[30:31], 0xfffff
	v_mov_b64_e32 v[10:11], v[20:21]
	v_readlane_b32 s37, v253, 27
	v_readlane_b32 s40, v253, 30
	v_readlane_b32 s41, v253, 31
	v_readlane_b32 s44, v253, 34
	v_readlane_b32 s45, v253, 35
	v_readlane_b32 s46, v253, 36
	v_readlane_b32 s47, v253, 37
	v_readlane_b32 s48, v253, 38
	v_readlane_b32 s49, v253, 39
	v_readlane_b32 s50, v253, 40
	v_readlane_b32 s51, v253, 41
	s_cmp_lg_u32 s16, 0x20000
	s_cbranch_scc1 .LBB0_45
	v_and_b32_e32 v8, 0x20000, v10
	v_lshrrev_b32_e32 v16, 13, v10
	v_lshrrev_b32_e32 v15, 12, v10
	v_cmp_eq_u64_e32 vcc, 0, v[8:9]
	v_and_b32_e32 v8, 0x60, v16
	v_and_or_b32 v8, v15, 31, v8
	v_and_b32_e32 v18, 0xfc0, v6
	v_cndmask_b32_e32 v17, v1, v12, vcc
	v_cndmask_b32_e32 v16, v13, v14, vcc
	v_lshlrev_b32_e32 v8, 14, v8
	v_lshrrev_b32_e32 v19, 4, v10
	v_lshl_add_u64 v[16:17], v[16:17], 0, v[8:9]
	v_lshlrev_b32_e32 v8, 2, v18
	v_lshl_add_u64 v[16:17], v[16:17], 0, v[8:9]
	v_and_b32_e32 v8, 0xfc, v19
	v_lshl_add_u64 v[16:17], v[16:17], 0, v[8:9]
	global_load_dword v130, v[16:17], off
	v_lshl_add_u64 v[10:11], v[10:11], 0, s[16:17]
	v_lshl_add_u64 v[6:7], v[6:7], 0, s[18:19]
	v_and_b32_e32 v8, 0x20000, v10
	v_lshrrev_b32_e32 v16, 13, v10
	v_lshrrev_b32_e32 v15, 12, v10
	v_cmp_eq_u64_e32 vcc, 0, v[8:9]
	v_and_b32_e32 v8, 0x60, v16
	v_and_or_b32 v8, v15, 31, v8
	v_and_b32_e32 v18, 0xfc0, v6
	v_cndmask_b32_e32 v17, v1, v12, vcc
	v_cndmask_b32_e32 v16, v13, v14, vcc
	v_lshlrev_b32_e32 v8, 14, v8
	v_lshrrev_b32_e32 v19, 4, v10
	v_lshl_add_u64 v[16:17], v[16:17], 0, v[8:9]
	v_lshlrev_b32_e32 v8, 2, v18
	v_lshl_add_u64 v[16:17], v[16:17], 0, v[8:9]
	v_and_b32_e32 v8, 0xfc, v19
	v_lshl_add_u64 v[16:17], v[16:17], 0, v[8:9]
	global_load_dword v131, v[16:17], off
	v_lshl_add_u64 v[10:11], v[10:11], 0, s[16:17]
	v_lshl_add_u64 v[6:7], v[6:7], 0, s[18:19]
	v_and_b32_e32 v8, 0x20000, v10
	v_lshrrev_b32_e32 v16, 13, v10
	v_lshrrev_b32_e32 v15, 12, v10
	v_cmp_eq_u64_e32 vcc, 0, v[8:9]
	v_and_b32_e32 v8, 0x60, v16
	v_and_or_b32 v8, v15, 31, v8
	v_and_b32_e32 v18, 0xfc0, v6
	v_cndmask_b32_e32 v17, v1, v12, vcc
	v_cndmask_b32_e32 v16, v13, v14, vcc
	v_lshlrev_b32_e32 v8, 14, v8
	v_lshrrev_b32_e32 v19, 4, v10
	v_lshl_add_u64 v[16:17], v[16:17], 0, v[8:9]
	v_lshlrev_b32_e32 v8, 2, v18
	v_lshl_add_u64 v[16:17], v[16:17], 0, v[8:9]
	v_and_b32_e32 v8, 0xfc, v19
	v_lshl_add_u64 v[16:17], v[16:17], 0, v[8:9]
	global_load_dword v132, v[16:17], off
	v_lshl_add_u64 v[10:11], v[10:11], 0, s[16:17]
	v_lshl_add_u64 v[6:7], v[6:7], 0, s[18:19]
	v_and_b32_e32 v8, 0x20000, v10
	v_lshrrev_b32_e32 v16, 13, v10
	v_lshrrev_b32_e32 v15, 12, v10
	v_cmp_eq_u64_e32 vcc, 0, v[8:9]
	v_and_b32_e32 v8, 0x60, v16
	v_and_or_b32 v8, v15, 31, v8
	v_and_b32_e32 v18, 0xfc0, v6
	v_cndmask_b32_e32 v17, v1, v12, vcc
	v_cndmask_b32_e32 v16, v13, v14, vcc
	v_lshlrev_b32_e32 v8, 14, v8
	v_lshrrev_b32_e32 v19, 4, v10
	v_lshl_add_u64 v[16:17], v[16:17], 0, v[8:9]
	v_lshlrev_b32_e32 v8, 2, v18
	v_lshl_add_u64 v[16:17], v[16:17], 0, v[8:9]
	v_and_b32_e32 v8, 0xfc, v19
	v_lshl_add_u64 v[16:17], v[16:17], 0, v[8:9]
	global_load_dword v133, v[16:17], off
	v_lshl_add_u64 v[10:11], v[10:11], 0, s[16:17]
	v_lshl_add_u64 v[6:7], v[6:7], 0, s[18:19]
	v_and_b32_e32 v8, 0x20000, v10
	v_lshrrev_b32_e32 v16, 13, v10
	v_lshrrev_b32_e32 v15, 12, v10
	v_cmp_eq_u64_e32 vcc, 0, v[8:9]
	v_and_b32_e32 v8, 0x60, v16
	v_and_or_b32 v8, v15, 31, v8
	v_and_b32_e32 v18, 0xfc0, v6
	v_cndmask_b32_e32 v17, v1, v12, vcc
	v_cndmask_b32_e32 v16, v13, v14, vcc
	v_lshlrev_b32_e32 v8, 14, v8
	v_lshrrev_b32_e32 v19, 4, v10
	v_lshl_add_u64 v[16:17], v[16:17], 0, v[8:9]
	v_lshlrev_b32_e32 v8, 2, v18
	v_lshl_add_u64 v[16:17], v[16:17], 0, v[8:9]
	v_and_b32_e32 v8, 0xfc, v19
	v_lshl_add_u64 v[16:17], v[16:17], 0, v[8:9]
	global_load_dword v134, v[16:17], off
	v_lshl_add_u64 v[10:11], v[10:11], 0, s[16:17]
	v_lshl_add_u64 v[6:7], v[6:7], 0, s[18:19]
	v_and_b32_e32 v8, 0x20000, v10
	v_lshrrev_b32_e32 v16, 13, v10
	v_lshrrev_b32_e32 v15, 12, v10
	v_cmp_eq_u64_e32 vcc, 0, v[8:9]
	v_and_b32_e32 v8, 0x60, v16
	v_and_or_b32 v8, v15, 31, v8
	v_and_b32_e32 v18, 0xfc0, v6
	v_cndmask_b32_e32 v17, v1, v12, vcc
	v_cndmask_b32_e32 v16, v13, v14, vcc
	v_lshlrev_b32_e32 v8, 14, v8
	v_lshrrev_b32_e32 v19, 4, v10
	v_lshl_add_u64 v[16:17], v[16:17], 0, v[8:9]
	v_lshlrev_b32_e32 v8, 2, v18
	v_lshl_add_u64 v[16:17], v[16:17], 0, v[8:9]
	v_and_b32_e32 v8, 0xfc, v19
	v_lshl_add_u64 v[16:17], v[16:17], 0, v[8:9]
	global_load_dword v135, v[16:17], off
	v_lshl_add_u64 v[10:11], v[10:11], 0, s[16:17]
	v_lshl_add_u64 v[6:7], v[6:7], 0, s[18:19]
	v_and_b32_e32 v8, 0x20000, v10
	v_lshrrev_b32_e32 v16, 13, v10
	v_lshrrev_b32_e32 v15, 12, v10
	v_cmp_eq_u64_e32 vcc, 0, v[8:9]
	v_and_b32_e32 v8, 0x60, v16
	v_and_or_b32 v8, v15, 31, v8
	v_and_b32_e32 v18, 0xfc0, v6
	v_cndmask_b32_e32 v17, v1, v12, vcc
	v_cndmask_b32_e32 v16, v13, v14, vcc
	v_lshlrev_b32_e32 v8, 14, v8
	v_lshrrev_b32_e32 v19, 4, v10
	v_lshl_add_u64 v[16:17], v[16:17], 0, v[8:9]
	v_lshlrev_b32_e32 v8, 2, v18
	v_lshl_add_u64 v[16:17], v[16:17], 0, v[8:9]
	v_and_b32_e32 v8, 0xfc, v19
	v_lshl_add_u64 v[16:17], v[16:17], 0, v[8:9]
	global_load_dword v136, v[16:17], off
	v_lshl_add_u64 v[10:11], v[10:11], 0, s[16:17]
	v_lshl_add_u64 v[6:7], v[6:7], 0, s[18:19]
	v_and_b32_e32 v8, 0x20000, v10
	v_lshrrev_b32_e32 v16, 13, v10
	v_lshrrev_b32_e32 v15, 12, v10
	v_cmp_eq_u64_e32 vcc, 0, v[8:9]
	v_and_b32_e32 v8, 0x60, v16
	v_and_or_b32 v8, v15, 31, v8
	v_and_b32_e32 v18, 0xfc0, v6
	v_cndmask_b32_e32 v17, v1, v12, vcc
	v_cndmask_b32_e32 v16, v13, v14, vcc
	v_lshlrev_b32_e32 v8, 14, v8
	v_lshrrev_b32_e32 v19, 4, v10
	v_lshl_add_u64 v[16:17], v[16:17], 0, v[8:9]
	v_lshlrev_b32_e32 v8, 2, v18
	v_lshl_add_u64 v[16:17], v[16:17], 0, v[8:9]
	v_and_b32_e32 v8, 0xfc, v19
	v_lshl_add_u64 v[16:17], v[16:17], 0, v[8:9]
	global_load_dword v137, v[16:17], off
	v_lshl_add_u64 v[10:11], v[10:11], 0, s[16:17]
	v_lshl_add_u64 v[6:7], v[6:7], 0, s[18:19]
	s_waitcnt vmcnt(7)
	v_bfe_u32 v15, v130, 16, 1
	v_add3_u32 v15, v130, v15, s22
	global_store_short_d16_hi v[4:5], v15, off
	v_lshl_add_u64 v[4:5], v[4:5], 0, s[2:3]
	s_waitcnt vmcnt(7)
	v_bfe_u32 v15, v131, 16, 1
	v_add3_u32 v15, v131, v15, s22
	global_store_short_d16_hi v[4:5], v15, off
	v_lshl_add_u64 v[4:5], v[4:5], 0, s[2:3]
	s_waitcnt vmcnt(7)
	v_bfe_u32 v15, v132, 16, 1
	v_add3_u32 v15, v132, v15, s22
	global_store_short_d16_hi v[4:5], v15, off
	v_lshl_add_u64 v[4:5], v[4:5], 0, s[2:3]
	s_waitcnt vmcnt(7)
	v_bfe_u32 v15, v133, 16, 1
	v_add3_u32 v15, v133, v15, s22
	global_store_short_d16_hi v[4:5], v15, off
	v_lshl_add_u64 v[4:5], v[4:5], 0, s[2:3]
	s_waitcnt vmcnt(7)
	v_bfe_u32 v15, v134, 16, 1
	v_add3_u32 v15, v134, v15, s22
	global_store_short_d16_hi v[4:5], v15, off
	v_lshl_add_u64 v[4:5], v[4:5], 0, s[2:3]
	s_waitcnt vmcnt(7)
	v_bfe_u32 v15, v135, 16, 1
	v_add3_u32 v15, v135, v15, s22
	global_store_short_d16_hi v[4:5], v15, off
	v_lshl_add_u64 v[4:5], v[4:5], 0, s[2:3]
	s_waitcnt vmcnt(7)
	v_bfe_u32 v15, v136, 16, 1
	v_add3_u32 v15, v136, v15, s22
	global_store_short_d16_hi v[4:5], v15, off
	v_lshl_add_u64 v[4:5], v[4:5], 0, s[2:3]
	s_waitcnt vmcnt(7)
	v_bfe_u32 v15, v137, 16, 1
	v_add3_u32 v15, v137, v15, s22
	global_store_short_d16_hi v[4:5], v15, off
	v_lshl_add_u64 v[4:5], v[4:5], 0, s[2:3]
	s_branch .LBB0_46

.LBB0_46:
	s_or_b64 exec, exec, s[0:1]
	s_mov_b64 s[0:1], 0x80000
	v_cmp_gt_u64_e32 vcc, s[0:1], v[20:21]
	s_and_saveexec_b64 s[0:1], vcc
	v_readlane_b32 s36, v253, 42
	v_readlane_b32 s37, v253, 43
	v_readlane_b32 s40, v253, 46
	v_readlane_b32 s41, v253, 47
	v_readlane_b32 s38, v253, 44
	v_readlane_b32 s39, v253, 45
	v_readlane_b32 s42, v253, 48
	v_readlane_b32 s43, v253, 49
	v_readlane_b32 s44, v253, 50
	v_readlane_b32 s45, v253, 51
	v_readlane_b32 s46, v253, 52
	v_readlane_b32 s47, v253, 53
	v_readlane_b32 s48, v253, 54
	v_readlane_b32 s49, v253, 55
	v_readlane_b32 s50, v253, 56
	v_readlane_b32 s51, v253, 57
	s_cbranch_execz .LBB0_49
	s_lshl_b64 s[2:3], s[12:13], 10
	s_add_u32 s2, s10, s2
	s_addc_u32 s3, s11, s3
	v_lshl_add_u64 v[4:5], v[2:3], 1, s[2:3]
	s_mov_b64 s[2:3], 0xa800000
	s_lshl_b64 s[18:19], s[12:13], 19
	v_lshlrev_b64 v[6:7], 10, v[2:3]
	v_lshl_add_u64 v[4:5], v[4:5], 0, s[2:3]
	s_lshl_b64 s[2:3], s[14:15], 10
	v_lshl_add_u64 v[6:7], s[18:19], 0, v[6:7]
	s_lshl_b64 s[18:19], s[14:15], 19
	s_mov_b64 s[28:29], 0
	s_movk_i32 s22, 0x7fff
	s_mov_b64 s[30:31], 0x7ffff
	v_mov_b64_e32 v[8:9], v[20:21]
	s_cmp_lg_u32 s16, 0x20000
	s_cbranch_scc1 .LBB0_48
	v_bfe_u32 v1, v8, 6, 10
	v_and_b32_e32 v10, 0xfc00, v6
	v_and_b32_e32 v11, 0x70000, v8
	v_or3_b32 v1, v10, v11, v1
	v_lshlrev_b32_e32 v1, 2, v1
	global_load_dword v140, v1, s[36:37]
	global_load_dword v141, v1, s[40:41]
	v_lshl_add_u64 v[8:9], v[8:9], 0, s[16:17]
	v_lshl_add_u64 v[6:7], v[6:7], 0, s[18:19]
	v_bfe_u32 v1, v8, 6, 10
	v_and_b32_e32 v10, 0xfc00, v6
	v_and_b32_e32 v11, 0x70000, v8
	v_or3_b32 v1, v10, v11, v1
	v_lshlrev_b32_e32 v1, 2, v1
	global_load_dword v142, v1, s[36:37]
	global_load_dword v143, v1, s[40:41]
	v_lshl_add_u64 v[8:9], v[8:9], 0, s[16:17]
	v_lshl_add_u64 v[6:7], v[6:7], 0, s[18:19]
	v_bfe_u32 v1, v8, 6, 10
	v_and_b32_e32 v10, 0xfc00, v6
	v_and_b32_e32 v11, 0x70000, v8
	v_or3_b32 v1, v10, v11, v1
	v_lshlrev_b32_e32 v1, 2, v1
	global_load_dword v144, v1, s[36:37]
	global_load_dword v145, v1, s[40:41]
	v_lshl_add_u64 v[8:9], v[8:9], 0, s[16:17]
	v_lshl_add_u64 v[6:7], v[6:7], 0, s[18:19]
	v_bfe_u32 v1, v8, 6, 10
	v_and_b32_e32 v10, 0xfc00, v6
	v_and_b32_e32 v11, 0x70000, v8
	v_or3_b32 v1, v10, v11, v1
	v_lshlrev_b32_e32 v1, 2, v1
	global_load_dword v146, v1, s[36:37]
	global_load_dword v147, v1, s[40:41]
	v_lshl_add_u64 v[8:9], v[8:9], 0, s[16:17]
	v_lshl_add_u64 v[6:7], v[6:7], 0, s[18:19]
	v_add_co_u32_e32 v10, vcc, 0xfff00000, v4
	s_waitcnt vmcnt(6)
	v_bfe_u32 v13, v140, 16, 1
	v_addc_co_u32_e32 v11, vcc, -1, v5, vcc
	v_bfe_u32 v14, v141, 16, 1
	v_add3_u32 v13, v140, v13, s22
	v_add3_u32 v14, v141, v14, s22
	global_store_short_d16_hi v[10:11], v13, off
	global_store_short_d16_hi v[4:5], v14, off
	v_lshl_add_u64 v[4:5], v[4:5], 0, s[2:3]
	v_add_co_u32_e32 v10, vcc, 0xfff00000, v4
	s_waitcnt vmcnt(6)
	v_bfe_u32 v13, v142, 16, 1
	v_addc_co_u32_e32 v11, vcc, -1, v5, vcc
	v_bfe_u32 v14, v143, 16, 1
	v_add3_u32 v13, v142, v13, s22
	v_add3_u32 v14, v143, v14, s22
	global_store_short_d16_hi v[10:11], v13, off
	global_store_short_d16_hi v[4:5], v14, off
	v_lshl_add_u64 v[4:5], v[4:5], 0, s[2:3]
	v_add_co_u32_e32 v10, vcc, 0xfff00000, v4
	s_waitcnt vmcnt(6)
	v_bfe_u32 v13, v144, 16, 1
	v_addc_co_u32_e32 v11, vcc, -1, v5, vcc
	v_bfe_u32 v14, v145, 16, 1
	v_add3_u32 v13, v144, v13, s22
	v_add3_u32 v14, v145, v14, s22
	global_store_short_d16_hi v[10:11], v13, off
	global_store_short_d16_hi v[4:5], v14, off
	v_lshl_add_u64 v[4:5], v[4:5], 0, s[2:3]
	v_add_co_u32_e32 v10, vcc, 0xfff00000, v4
	s_waitcnt vmcnt(6)
	v_bfe_u32 v13, v146, 16, 1
	v_addc_co_u32_e32 v11, vcc, -1, v5, vcc
	v_bfe_u32 v14, v147, 16, 1
	v_add3_u32 v13, v146, v13, s22
	v_add3_u32 v14, v147, v14, s22
	global_store_short_d16_hi v[10:11], v13, off
	global_store_short_d16_hi v[4:5], v14, off
	v_lshl_add_u64 v[4:5], v[4:5], 0, s[2:3]
	s_branch .LBB0_49

.LBB0_49:
	s_or_b64 exec, exec, s[0:1]
	s_mov_b64 s[0:1], 0xa0000
	v_cmp_gt_u64_e32 vcc, s[0:1], v[20:21]
	s_and_saveexec_b64 s[0:1], vcc
	v_readlane_b32 s36, v253, 42
	v_readlane_b32 s42, v253, 48
	v_readlane_b32 s43, v253, 49
	v_readlane_b32 s37, v253, 43
	v_readlane_b32 s38, v253, 44
	v_readlane_b32 s39, v253, 45
	v_readlane_b32 s40, v253, 46
	v_readlane_b32 s41, v253, 47
	v_readlane_b32 s44, v253, 50
	v_readlane_b32 s45, v253, 51
	v_readlane_b32 s46, v253, 52
	v_readlane_b32 s47, v253, 53
	v_readlane_b32 s48, v253, 54
	v_readlane_b32 s49, v253, 55
	v_readlane_b32 s50, v253, 56
	v_readlane_b32 s51, v253, 57
	s_cbranch_execz .LBB0_52
	s_lshl_b64 s[2:3], s[12:13], 10
	s_add_u32 s2, s10, s2
	s_addc_u32 s3, s11, s3
	v_lshl_add_u64 v[4:5], v[2:3], 1, s[2:3]
	s_mov_b64 s[2:3], 0xa900000
	v_lshl_add_u64 v[4:5], v[4:5], 0, s[2:3]
	s_lshl_b64 s[2:3], s[14:15], 10
	s_mov_b64 s[18:19], 0
	s_mov_b32 s22, 0xcccccccd
	v_mov_b32_e32 v7, 0
	s_movk_i32 s23, 0x7fff
	s_mov_b64 s[28:29], 0x9ffff
	v_mov_b64_e32 v[8:9], v[20:21]
	s_cmp_lg_u32 s16, 0x20000
	s_cbranch_scc1 .LBB0_51
	v_mul_hi_u32 v1, v8, s22
	v_lshrrev_b32_e32 v6, 7, v1
	v_lshrrev_b32_e32 v10, 17, v1
	v_mul_u32_u24_e32 v6, 0xa0, v6
	v_mul_u32_u24_e32 v10, 0xa0, v10
	v_sub_u32_e32 v6, v8, v6
	v_lshrrev_b32_e32 v1, 5, v1
	v_add_lshl_u32 v6, v10, v6, 12
	v_lshl_add_u64 v[10:11], s[42:43], 0, v[6:7]
	v_and_b32_e32 v6, 0xffc, v1
	v_lshl_add_u64 v[10:11], v[10:11], 0, v[6:7]
	global_load_dword v150, v[10:11], off
	v_lshl_add_u64 v[8:9], v[8:9], 0, s[16:17]
	v_mul_hi_u32 v1, v8, s22
	v_lshrrev_b32_e32 v6, 7, v1
	v_lshrrev_b32_e32 v10, 17, v1
	v_mul_u32_u24_e32 v6, 0xa0, v6
	v_mul_u32_u24_e32 v10, 0xa0, v10
	v_sub_u32_e32 v6, v8, v6
	v_lshrrev_b32_e32 v1, 5, v1
	v_add_lshl_u32 v6, v10, v6, 12
	v_lshl_add_u64 v[10:11], s[42:43], 0, v[6:7]
	v_and_b32_e32 v6, 0xffc, v1
	v_lshl_add_u64 v[10:11], v[10:11], 0, v[6:7]
	global_load_dword v151, v[10:11], off
	v_lshl_add_u64 v[8:9], v[8:9], 0, s[16:17]
	v_mul_hi_u32 v1, v8, s22
	v_lshrrev_b32_e32 v6, 7, v1
	v_lshrrev_b32_e32 v10, 17, v1
	v_mul_u32_u24_e32 v6, 0xa0, v6
	v_mul_u32_u24_e32 v10, 0xa0, v10
	v_sub_u32_e32 v6, v8, v6
	v_lshrrev_b32_e32 v1, 5, v1
	v_add_lshl_u32 v6, v10, v6, 12
	v_lshl_add_u64 v[10:11], s[42:43], 0, v[6:7]
	v_and_b32_e32 v6, 0xffc, v1
	v_lshl_add_u64 v[10:11], v[10:11], 0, v[6:7]
	global_load_dword v152, v[10:11], off
	v_lshl_add_u64 v[8:9], v[8:9], 0, s[16:17]
	v_mul_hi_u32 v1, v8, s22
	v_lshrrev_b32_e32 v6, 7, v1
	v_lshrrev_b32_e32 v10, 17, v1
	v_mul_u32_u24_e32 v6, 0xa0, v6
	v_mul_u32_u24_e32 v10, 0xa0, v10
	v_sub_u32_e32 v6, v8, v6
	v_lshrrev_b32_e32 v1, 5, v1
	v_add_lshl_u32 v6, v10, v6, 12
	v_lshl_add_u64 v[10:11], s[42:43], 0, v[6:7]
	v_and_b32_e32 v6, 0xffc, v1
	v_lshl_add_u64 v[10:11], v[10:11], 0, v[6:7]
	global_load_dword v153, v[10:11], off
	v_lshl_add_u64 v[8:9], v[8:9], 0, s[16:17]
	v_mul_hi_u32 v1, v8, s22
	v_lshrrev_b32_e32 v6, 7, v1
	v_lshrrev_b32_e32 v10, 17, v1
	v_mul_u32_u24_e32 v6, 0xa0, v6
	v_mul_u32_u24_e32 v10, 0xa0, v10
	v_sub_u32_e32 v6, v8, v6
	v_lshrrev_b32_e32 v1, 5, v1
	v_add_lshl_u32 v6, v10, v6, 12
	v_lshl_add_u64 v[10:11], s[42:43], 0, v[6:7]
	v_and_b32_e32 v6, 0xffc, v1
	v_lshl_add_u64 v[10:11], v[10:11], 0, v[6:7]
	global_load_dword v154, v[10:11], off
	v_lshl_add_u64 v[8:9], v[8:9], 0, s[16:17]
	s_waitcnt vmcnt(4)
	v_bfe_u32 v6, v150, 16, 1
	v_add3_u32 v6, v150, v6, s23
	global_store_short_d16_hi v[4:5], v6, off
	v_lshl_add_u64 v[4:5], v[4:5], 0, s[2:3]
	s_waitcnt vmcnt(4)
	v_bfe_u32 v6, v151, 16, 1
	v_add3_u32 v6, v151, v6, s23
	global_store_short_d16_hi v[4:5], v6, off
	v_lshl_add_u64 v[4:5], v[4:5], 0, s[2:3]
	s_waitcnt vmcnt(4)
	v_bfe_u32 v6, v152, 16, 1
	v_add3_u32 v6, v152, v6, s23
	global_store_short_d16_hi v[4:5], v6, off
	v_lshl_add_u64 v[4:5], v[4:5], 0, s[2:3]
	s_waitcnt vmcnt(4)
	v_bfe_u32 v6, v153, 16, 1
	v_add3_u32 v6, v153, v6, s23
	global_store_short_d16_hi v[4:5], v6, off
	v_lshl_add_u64 v[4:5], v[4:5], 0, s[2:3]
	s_waitcnt vmcnt(4)
	v_bfe_u32 v6, v154, 16, 1
	v_add3_u32 v6, v154, v6, s23
	global_store_short_d16_hi v[4:5], v6, off
	v_lshl_add_u64 v[4:5], v[4:5], 0, s[2:3]
	s_branch .LBB0_52
